# speedup vs baseline: 1.0228x; 1.0012x over previous
.LBB1_102:
	s_and_b64 s[16:17], s[18:19], s[16:17]
	s_andn2_b64 vcc, exec, s[16:17]
	s_waitcnt lgkmcnt(0)
	s_barrier
	s_cbranch_vccnz .LBB1_106
	s_and_saveexec_b64 s[16:17], s[2:3]
	s_cbranch_execz .LBB1_105
	v_add_u32_e32 v2, 0x8400, v60
	ds_read2_b32 v[0:1], v2 offset0:64 offset1:96
	ds_read2_b32 v[6:7], v2 offset0:128 offset1:160
	s_waitcnt lgkmcnt(1)
	v_add_f32_e32 v3, v0, v1
	s_waitcnt lgkmcnt(0)
	v_add_f32_e32 v0, v3, v6
	v_add_f32_e32 v0, v0, v7
	v_accvgpr_read_b32 v1, a238
	v_add_f32_e32 v0, v1, v0
	v_accvgpr_read_b32 v1, a239
	ds_write_b32 v1, v0 offset:33856

.LBB1_169:
	s_or_b64 exec, exec, s[16:17]
	s_waitcnt lgkmcnt(0)
	s_barrier
	s_and_saveexec_b64 s[16:17], s[6:7]
	s_cbranch_execz .LBB1_73
	v_add_u32_e32 v2, 0x8400, v60
	ds_read2_b32 v[0:1], v2 offset0:192 offset1:208
	ds_read2_b32 v[6:7], v2 offset0:224 offset1:240
	s_waitcnt lgkmcnt(1)
	v_add_f32_e32 v3, v0, v1
	s_waitcnt lgkmcnt(0)
	v_add_f32_e32 v0, v3, v6
	v_add_f32_e32 v0, v0, v7
	v_accvgpr_read_b32 v1, a142
	v_add_f32_e32 v0, v1, v0
	v_accvgpr_read_b32 v1, a143
	v_lshl_add_u32 v1, s41, 6, v1
	ds_write_b32 v1, v0
	ds_write_b32 v60, v0 offset:33792
	s_branch .LBB1_73
